# select v6: first block of the wave's next row requested during the last block of the final pass
# baseline (speedup 1.0000x reference)
.LBB0_1220:
	s_waitcnt lgkmcnt(0)
	s_barrier
	s_cmpk_gt_i32 s3, 0x1fff
	s_cbranch_scc1 .LBB0_1868
	s_add_u32 s46, s30, 0x17100000
	s_addc_u32 s47, s31, 0
	s_add_u32 s48, s30, 0x69b00000
	s_addc_u32 s49, s31, 0
	s_add_u32 s50, s30, 0x6a300000
	s_addc_u32 s51, s31, 0
	s_add_i32 s52, s2, 0
	s_cmpk_eq_i32 s84, 0x100
	s_waitcnt vmcnt(11)
	v_lshlrev_b64 v[2:3], v50, -1
	s_cselect_b64 s[18:19], -1, 0
	s_abs_i32 s54, s35
	v_not_b32_e32 v52, v2
	v_cvt_f32_u32_e32 v2, s54
	s_sub_i32 s2, 0, s54
	v_mov_b32_e32 v59, 0
	v_lshlrev_b32_e32 v54, 4, v50
	v_rcp_iflag_f32_e32 v2, v2
	v_mov_b32_e32 v55, v59
	v_not_b32_e32 v1, v3
	v_lshlrev_b32_e32 v56, 2, v50
	v_mul_f32_e32 v2, 0x4f7ffffe, v2
	v_cvt_u32_f32_e32 v2, v2
	v_mov_b32_e32 v57, v59
	s_mov_b64 s[4:5], 0x17100000
	v_lshlrev_b32_e32 v4, 7, v50
	v_readfirstlane_b32 s6, v2
	s_mul_i32 s2, s2, s6
	s_mul_hi_u32 s2, s6, s2
	s_add_i32 s56, s6, s2
	v_lshl_add_u64 v[2:3], s[30:31], 0, v[54:55]
	s_mov_b64 s[6:7], 0x17101000
	v_lshl_add_u64 v[60:61], v[2:3], 0, s[6:7]
	v_lshl_add_u64 v[2:3], s[30:31], 0, v[56:57]
	v_lshlrev_b32_e32 v53, 5, v50
	v_lshlrev_b32_e32 v5, 6, v50
	v_lshl_add_u64 v[62:63], v[2:3], 0, s[4:5]
	v_add_u32_e32 v2, s52, v56
	s_mov_b32 s12, 0
	s_movk_i32 s53, 0x100
	v_cmp_eq_u32_e64 s[0:1], 0, v50
	v_or_b32_e32 v66, 31, v53
	v_or_b32_e32 v67, 30, v53
	v_or_b32_e32 v68, 29, v53
	v_or_b32_e32 v69, 28, v53
	v_or_b32_e32 v70, 27, v53
	v_or_b32_e32 v71, 26, v53
	v_or_b32_e32 v72, 25, v53
	v_or_b32_e32 v73, 24, v53
	v_or_b32_e32 v74, 23, v53
	v_or_b32_e32 v75, 22, v53
	v_or_b32_e32 v76, 21, v53
	v_or_b32_e32 v77, 20, v53
	v_or_b32_e32 v78, 19, v53
	v_or_b32_e32 v79, 18, v53
	v_or_b32_e32 v80, 17, v53
	v_or_b32_e32 v81, 16, v53
	v_or_b32_e32 v82, 15, v53
	v_or_b32_e32 v83, 14, v53
	v_or_b32_e32 v84, 13, v53
	v_or_b32_e32 v85, 12, v53
	v_or_b32_e32 v86, 11, v53
	v_or_b32_e32 v87, 10, v53
	v_or_b32_e32 v88, 9, v53
	v_or_b32_e32 v89, 8, v53
	v_or_b32_e32 v90, 7, v53
	v_or_b32_e32 v91, 6, v53
	v_or_b32_e32 v92, 5, v53
	v_or_b32_e32 v93, 4, v53
	v_or_b32_e32 v94, 3, v53
	v_or_b32_e32 v95, 2, v53
	v_or_b32_e32 v96, 1, v53
	v_or_b32_e32 v97, 15, v54
	v_or_b32_e32 v98, 14, v54
	v_or_b32_e32 v99, 13, v54
	v_or_b32_e32 v100, 12, v54
	v_or_b32_e32 v101, 11, v54
	v_or_b32_e32 v102, 10, v54
	v_or_b32_e32 v103, 9, v54
	v_or_b32_e32 v104, 8, v54
	v_or_b32_e32 v105, 7, v54
	v_or_b32_e32 v106, 6, v54
	v_or_b32_e32 v107, 5, v54
	v_or_b32_e32 v108, 4, v54
	v_or_b32_e32 v109, 3, v54
	v_or_b32_e32 v110, 2, v54
	v_or_b32_e32 v111, 1, v54
	v_or_b32_e32 v112, 64, v50
	v_or_b32_e32 v113, 0x80, v50
	v_or_b32_e32 v114, 0xc0, v50
	s_ashr_i32 s55, s35, 31
	v_add_u32_e32 v55, 0x2000, v2
	s_movk_i32 s57, 0xff
	v_mov_b32_e32 v57, 1
	s_mov_b64 s[20:21], 0x1000
	s_mov_b64 s[22:23], 0x100
	v_add_u32_e32 v115, s52, v5
	v_lshlrev_b32_e32 v116, 2, v50
	v_add_u32_e32 v117, s52, v4
	s_mov_b32 s82, -1
	s_cmpk_eq_i32 s84, 0x100
	s_cbranch_scc0 .LBB0_1223
	s_and_b32 s4, s3, 7
	s_lshr_b32 s5, s4, 2
	s_lshl_b32 s5, s5, 1
	s_add_i32 s4, s4, s5
	s_and_b32 s4, s4, 3
	s_lshl_b32 s4, s4, 11
	s_add_i32 s3, s3, s4
	s_and_b32 s3, s3, 0x1fff
	s_mov_b32 s99, 4
	s_branch .LBB0_1223

.LBB0_1234:
	s_or_b64 exec, exec, s[4:5]
	s_lshl_b64 s[4:5], s[38:39], 10
	s_add_u32 s40, s48, s4
	s_addc_u32 s41, s49, s5
	s_cmpk_gt_i32 s38, 0xff
	s_mov_b64 s[4:5], -1
	s_cbranch_scc0 .LBB0_1866
	s_add_i32 s2, s38, 1
	s_lshl_b64 s[42:43], s[38:39], 15
	s_add_u32 s42, s46, s42
	s_addc_u32 s43, s47, s43
	v_lshlrev_b32_e32 v58, 4, v50
	v_add_u32_e32 v220, 0x1000, v58
	v_add_u32_e32 v221, 0x2000, v58
	v_add_u32_e32 v222, 0x3000, v58
	v_mov_b32_e32 v216, 0
	v_mov_b32_e32 v217, 0
	v_mov_b32_e32 v218, 0
	v_mov_b32_e32 v219, 0
	v_add_u32_e32 v64, s52, v58
	s_movk_i32 s15, 0x100
	s_cmp_eq_u32 s82, s38
	s_mov_b32 s82, -1
	s_cbranch_scc1 .Lsel_p1_have
	s_mov_b64 s[8:9], s[42:43]
	global_load_dwordx4 v[150:153], v58, s[8:9]
	s_cmp_le_i32 s2, 0x100
	s_cbranch_scc1 .Lsel_ld1_end
	global_load_dwordx4 v[154:157], v58, s[8:9] offset:1024
	s_cmp_le_i32 s2, 0x200
	s_cbranch_scc1 .Lsel_ld1_end
	global_load_dwordx4 v[158:161], v58, s[8:9] offset:2048
	s_cmp_le_i32 s2, 0x300
	s_cbranch_scc1 .Lsel_ld1_end
	global_load_dwordx4 v[162:165], v58, s[8:9] offset:3072
	s_cmp_le_i32 s2, 0x400
	s_cbranch_scc1 .Lsel_ld1_end
	global_load_dwordx4 v[166:169], v220, s[8:9]
	s_cmp_le_i32 s2, 0x500
	s_cbranch_scc1 .Lsel_ld1_end
	global_load_dwordx4 v[170:173], v220, s[8:9] offset:1024
	s_cmp_le_i32 s2, 0x600
	s_cbranch_scc1 .Lsel_ld1_end
	global_load_dwordx4 v[174:177], v220, s[8:9] offset:2048
	s_cmp_le_i32 s2, 0x700
	s_cbranch_scc1 .Lsel_ld1_end
	global_load_dwordx4 v[178:181], v220, s[8:9] offset:3072
	s_cmp_le_i32 s2, 0x800
	s_cbranch_scc1 .Lsel_ld1_end
	global_load_dwordx4 v[182:185], v221, s[8:9]
	s_cmp_le_i32 s2, 0x900
	s_cbranch_scc1 .Lsel_ld1_end
	global_load_dwordx4 v[186:189], v221, s[8:9] offset:1024
	s_cmp_le_i32 s2, 0xa00
	s_cbranch_scc1 .Lsel_ld1_end
	global_load_dwordx4 v[190:193], v221, s[8:9] offset:2048
	s_cmp_le_i32 s2, 0xb00
	s_cbranch_scc1 .Lsel_ld1_end
	global_load_dwordx4 v[194:197], v221, s[8:9] offset:3072
	s_cmp_le_i32 s2, 0xc00
	s_cbranch_scc1 .Lsel_ld1_end
	global_load_dwordx4 v[198:201], v222, s[8:9]
	s_cmp_le_i32 s2, 0xd00
	s_cbranch_scc1 .Lsel_ld1_end
	global_load_dwordx4 v[202:205], v222, s[8:9] offset:1024
	s_cmp_le_i32 s2, 0xe00
	s_cbranch_scc1 .Lsel_ld1_end
	global_load_dwordx4 v[206:209], v222, s[8:9] offset:2048
	s_cmp_le_i32 s2, 0xf00
	s_cbranch_scc1 .Lsel_ld1_end
	global_load_dwordx4 v[210:213], v222, s[8:9] offset:3072
.Lsel_ld1_end:
.Lsel_p1_have:
	s_mov_b64 s[8:9], s[42:43]
	ds_write_b128 v64, v[216:219]
	ds_write_b128 v64, v[216:219] offset:1024
	ds_write_b128 v64, v[216:219] offset:2048
	ds_write_b128 v64, v[216:219] offset:3072
	ds_write_b128 v64, v[216:219] offset:4096
	ds_write_b128 v64, v[216:219] offset:5120
	ds_write_b128 v64, v[216:219] offset:6144
	ds_write_b128 v64, v[216:219] offset:7168
	s_mov_b32 s16, 0
	s_waitcnt vmcnt(0)

.Lsel_fin_body:
	s_cmp_lt_i32 s36, s2
	s_cbranch_scc1 .Lsel_fin_nonext
	s_cmpk_eq_i32 s84, 0x100
	s_cbranch_scc0 .Lsel_fin_nonext
	s_cmp_lt_u32 s99, 2
	s_cbranch_scc1 .Lsel_fin_nonext
	s_add_i32 s4, s3, s35
	s_and_b32 s4, s4, 0x1fff
	s_and_b32 s5, s4, 0x7ff
	s_lshr_b32 s6, s4, 11
	s_sub_i32 s7, 0xfff, s5
	s_bitcmp1_b32 s6, 0
	s_cselect_b32 s5, s7, s5
	s_lshr_b32 s6, s6, 1
	s_lshl_b32 s6, s6, 12
	s_add_i32 s81, s5, s6
	s_cmpk_lt_i32 s81, 0x100
	s_cbranch_scc1 .Lsel_fin_nonext
	s_mov_b32 s82, s81
	s_lshl_b32 s7, s81, 15
	s_add_u32 s8, s46, s7
	s_addc_u32 s9, s47, 0
	s_add_i32 s83, s81, 1
	global_load_dwordx4 v[150:153], v58, s[8:9]
	s_cmp_le_i32 s83, 0x100
	s_cbranch_scc1 .Lsel_ld7_end
	global_load_dwordx4 v[154:157], v58, s[8:9] offset:1024
	s_cmp_le_i32 s83, 0x200
	s_cbranch_scc1 .Lsel_ld7_end
	global_load_dwordx4 v[158:161], v58, s[8:9] offset:2048
	s_cmp_le_i32 s83, 0x300
	s_cbranch_scc1 .Lsel_ld7_end
	global_load_dwordx4 v[162:165], v58, s[8:9] offset:3072
	s_cmp_le_i32 s83, 0x400
	s_cbranch_scc1 .Lsel_ld7_end
	global_load_dwordx4 v[166:169], v220, s[8:9]
	s_cmp_le_i32 s83, 0x500
	s_cbranch_scc1 .Lsel_ld7_end
	global_load_dwordx4 v[170:173], v220, s[8:9] offset:1024
	s_cmp_le_i32 s83, 0x600
	s_cbranch_scc1 .Lsel_ld7_end
	global_load_dwordx4 v[174:177], v220, s[8:9] offset:2048
	s_cmp_le_i32 s83, 0x700
	s_cbranch_scc1 .Lsel_ld7_end
	global_load_dwordx4 v[178:181], v220, s[8:9] offset:3072
	s_cmp_le_i32 s83, 0x800
	s_cbranch_scc1 .Lsel_ld7_end
	global_load_dwordx4 v[182:185], v221, s[8:9]
	s_cmp_le_i32 s83, 0x900
	s_cbranch_scc1 .Lsel_ld7_end
	global_load_dwordx4 v[186:189], v221, s[8:9] offset:1024
	s_cmp_le_i32 s83, 0xa00
	s_cbranch_scc1 .Lsel_ld7_end
	global_load_dwordx4 v[190:193], v221, s[8:9] offset:2048
	s_cmp_le_i32 s83, 0xb00
	s_cbranch_scc1 .Lsel_ld7_end
	global_load_dwordx4 v[194:197], v221, s[8:9] offset:3072
	s_cmp_le_i32 s83, 0xc00
	s_cbranch_scc1 .Lsel_ld7_end
	global_load_dwordx4 v[198:201], v222, s[8:9]
	s_cmp_le_i32 s83, 0xd00
	s_cbranch_scc1 .Lsel_ld7_end
	global_load_dwordx4 v[202:205], v222, s[8:9] offset:1024
	s_cmp_le_i32 s83, 0xe00
	s_cbranch_scc1 .Lsel_ld7_end
	global_load_dwordx4 v[206:209], v222, s[8:9] offset:2048
	s_cmp_le_i32 s83, 0xf00
	s_cbranch_scc1 .Lsel_ld7_end
	global_load_dwordx4 v[210:213], v222, s[8:9] offset:3072
.Lsel_ld7_end:
.Lsel_fin_nonext:
	v_add_u32_e32 v141, s16, v56
	v_ashrrev_i32_e32 v224, 31, v2
	v_or_b32_e32 v224, 0x80000000, v224
	v_xor_b32_e32 v224, v2, v224
	v_ashrrev_i32_e32 v225, 31, v3
	v_or_b32_e32 v225, 0x80000000, v225
	v_xor_b32_e32 v225, v3, v225
	v_ashrrev_i32_e32 v226, 31, v4
	v_or_b32_e32 v226, 0x80000000, v226
	v_xor_b32_e32 v226, v4, v226
	v_ashrrev_i32_e32 v227, 31, v5
	v_or_b32_e32 v227, 0x80000000, v227
	v_xor_b32_e32 v227, v5, v227
	v_cmp_lt_u32_e64 s[58:59], s17, v224
	v_cmp_eq_u32_e64 s[66:67], s17, v224
	v_cmp_lt_u32_e64 s[60:61], s17, v225
	v_cmp_eq_u32_e64 s[68:69], s17, v225
	v_cmp_lt_u32_e64 s[62:63], s17, v226
	v_cmp_eq_u32_e64 s[72:73], s17, v226
	v_cmp_lt_u32_e64 s[64:65], s17, v227
	v_cmp_eq_u32_e64 s[74:75], s17, v227
	s_or_b64 s[4:5], s[66:67], s[68:69]
	s_or_b64 s[6:7], s[72:73], s[74:75]
	s_or_b64 s[4:5], s[4:5], s[6:7]
	s_cmp_lg_u64 s[4:5], 0
	s_cbranch_scc0 .Lsel_fg_st0
	v_mov_b32_e32 v140, s27
	v_mbcnt_lo_u32_b32 v140, s66, v140
	v_mbcnt_hi_u32_b32 v140, s67, v140
	v_mbcnt_lo_u32_b32 v140, s68, v140
	v_mbcnt_hi_u32_b32 v140, s69, v140
	v_mbcnt_lo_u32_b32 v140, s72, v140
	v_mbcnt_hi_u32_b32 v140, s73, v140
	v_mbcnt_lo_u32_b32 v140, s74, v140
	v_mbcnt_hi_u32_b32 v140, s75, v140
	s_mov_b64 exec, s[66:67]
	v_cmp_gt_u32_e64 s[4:5], s15, v140
	v_add_u32_e32 v140, 1, v140
	s_or_b64 s[58:59], s[58:59], s[4:5]
	s_mov_b64 exec, s[68:69]
	v_cmp_gt_u32_e64 s[4:5], s15, v140
	v_add_u32_e32 v140, 1, v140
	s_or_b64 s[60:61], s[60:61], s[4:5]
	s_mov_b64 exec, s[72:73]
	v_cmp_gt_u32_e64 s[4:5], s15, v140
	v_add_u32_e32 v140, 1, v140
	s_or_b64 s[62:63], s[62:63], s[4:5]
	s_mov_b64 exec, s[74:75]
	v_cmp_gt_u32_e64 s[4:5], s15, v140
	v_add_u32_e32 v140, 1, v140
	s_or_b64 s[64:65], s[64:65], s[4:5]
	s_mov_b64 exec, -1
	s_bcnt1_i32_b64 s4, s[66:67]
	s_add_i32 s27, s27, s4
	s_bcnt1_i32_b64 s4, s[68:69]
	s_add_i32 s27, s27, s4
	s_bcnt1_i32_b64 s4, s[72:73]
	s_add_i32 s27, s27, s4
	s_bcnt1_i32_b64 s4, s[74:75]
	s_add_i32 s27, s27, s4

.Lsel_ld9_end:
.Lsel_fsp_nonext:
	v_add_u32_e32 v141, s16, v56
	v_cmp_ge_i32_e64 s[58:59], v2, s76
	v_cmp_ge_i32_e64 s[60:61], v3, s76
	v_cmp_ge_i32_e64 s[62:63], v4, s76
	v_cmp_ge_i32_e64 s[64:65], v5, s76
	v_mov_b32_e32 v139, s26
	v_mbcnt_lo_u32_b32 v139, s58, v139
	v_mbcnt_hi_u32_b32 v139, s59, v139
	v_mbcnt_lo_u32_b32 v139, s60, v139
	v_mbcnt_hi_u32_b32 v139, s61, v139
	v_mbcnt_lo_u32_b32 v139, s62, v139
	v_mbcnt_hi_u32_b32 v139, s63, v139
	v_mbcnt_lo_u32_b32 v139, s64, v139
	v_mbcnt_hi_u32_b32 v139, s65, v139
	v_lshlrev_b32_e32 v139, 2, v139
	s_mov_b64 exec, s[58:59]
	v_add_u32_e32 v142, 0, v141
	global_store_dword v139, v142, s[40:41]
	v_add_u32_e32 v139, 4, v139
	s_mov_b64 exec, s[60:61]
	v_add_u32_e32 v143, 1, v141
	global_store_dword v139, v143, s[40:41]
	v_add_u32_e32 v139, 4, v139
	s_mov_b64 exec, s[62:63]
	v_add_u32_e32 v144, 2, v141
	global_store_dword v139, v144, s[40:41]
	v_add_u32_e32 v139, 4, v139
	s_mov_b64 exec, s[64:65]
	v_add_u32_e32 v145, 3, v141
	global_store_dword v139, v145, s[40:41]
	v_add_u32_e32 v139, 4, v139
	s_mov_b64 exec, -1
	s_bcnt1_i32_b64 s4, s[58:59]
	s_add_i32 s26, s26, s4
	s_bcnt1_i32_b64 s4, s[60:61]
	s_add_i32 s26, s26, s4
	s_bcnt1_i32_b64 s4, s[62:63]
	s_add_i32 s26, s26, s4
	s_bcnt1_i32_b64 s4, s[64:65]
	s_add_i32 s26, s26, s4
	s_cmp_le_u32 s79, 1
	s_cbranch_scc1 .Lsel_fsp_bend
	v_cmp_ge_i32_e64 s[58:59], v6, s76
	v_cmp_ge_i32_e64 s[60:61], v7, s76
	v_cmp_ge_i32_e64 s[62:63], v8, s76
	v_cmp_ge_i32_e64 s[64:65], v9, s76
	v_mov_b32_e32 v139, s26
	v_mbcnt_lo_u32_b32 v139, s58, v139
	v_mbcnt_hi_u32_b32 v139, s59, v139
	v_mbcnt_lo_u32_b32 v139, s60, v139
	v_mbcnt_hi_u32_b32 v139, s61, v139
	v_mbcnt_lo_u32_b32 v139, s62, v139
	v_mbcnt_hi_u32_b32 v139, s63, v139
	v_mbcnt_lo_u32_b32 v139, s64, v139
	v_mbcnt_hi_u32_b32 v139, s65, v139
	v_lshlrev_b32_e32 v139, 2, v139
	s_mov_b64 exec, s[58:59]
	v_add_u32_e32 v142, 0x100, v141
	global_store_dword v139, v142, s[40:41]
	v_add_u32_e32 v139, 4, v139
	s_mov_b64 exec, s[60:61]
	v_add_u32_e32 v143, 0x101, v141
	global_store_dword v139, v143, s[40:41]
	v_add_u32_e32 v139, 4, v139
	s_mov_b64 exec, s[62:63]
	v_add_u32_e32 v144, 0x102, v141
	global_store_dword v139, v144, s[40:41]
	v_add_u32_e32 v139, 4, v139
	s_mov_b64 exec, s[64:65]
	v_add_u32_e32 v145, 0x103, v141
	global_store_dword v139, v145, s[40:41]
	v_add_u32_e32 v139, 4, v139
	s_mov_b64 exec, -1
	s_bcnt1_i32_b64 s4, s[58:59]
	s_add_i32 s26, s26, s4
	s_bcnt1_i32_b64 s4, s[60:61]
	s_add_i32 s26, s26, s4
	s_bcnt1_i32_b64 s4, s[62:63]
	s_add_i32 s26, s26, s4
	s_bcnt1_i32_b64 s4, s[64:65]
	s_add_i32 s26, s26, s4
	s_cmp_le_u32 s79, 2
	s_cbranch_scc1 .Lsel_fsp_bend
	v_cmp_ge_i32_e64 s[58:59], v10, s76
	v_cmp_ge_i32_e64 s[60:61], v11, s76
	v_cmp_ge_i32_e64 s[62:63], v12, s76
	v_cmp_ge_i32_e64 s[64:65], v13, s76
	v_mov_b32_e32 v139, s26
	v_mbcnt_lo_u32_b32 v139, s58, v139
	v_mbcnt_hi_u32_b32 v139, s59, v139
	v_mbcnt_lo_u32_b32 v139, s60, v139
	v_mbcnt_hi_u32_b32 v139, s61, v139
	v_mbcnt_lo_u32_b32 v139, s62, v139
	v_mbcnt_hi_u32_b32 v139, s63, v139
	v_mbcnt_lo_u32_b32 v139, s64, v139
	v_mbcnt_hi_u32_b32 v139, s65, v139
	v_lshlrev_b32_e32 v139, 2, v139
	s_mov_b64 exec, s[58:59]
	v_add_u32_e32 v142, 0x200, v141
	global_store_dword v139, v142, s[40:41]
	v_add_u32_e32 v139, 4, v139
	s_mov_b64 exec, s[60:61]
	v_add_u32_e32 v143, 0x201, v141
	global_store_dword v139, v143, s[40:41]
	v_add_u32_e32 v139, 4, v139
	s_mov_b64 exec, s[62:63]
	v_add_u32_e32 v144, 0x202, v141
	global_store_dword v139, v144, s[40:41]
	v_add_u32_e32 v139, 4, v139
	s_mov_b64 exec, s[64:65]
	v_add_u32_e32 v145, 0x203, v141
	global_store_dword v139, v145, s[40:41]
	v_add_u32_e32 v139, 4, v139
	s_mov_b64 exec, -1
	s_bcnt1_i32_b64 s4, s[58:59]
	s_add_i32 s26, s26, s4
	s_bcnt1_i32_b64 s4, s[60:61]
	s_add_i32 s26, s26, s4
	s_bcnt1_i32_b64 s4, s[62:63]
	s_add_i32 s26, s26, s4
	s_bcnt1_i32_b64 s4, s[64:65]
	s_add_i32 s26, s26, s4
	s_cmp_le_u32 s79, 3
	s_cbranch_scc1 .Lsel_fsp_bend
	v_cmp_ge_i32_e64 s[58:59], v14, s76
	v_cmp_ge_i32_e64 s[60:61], v15, s76
	v_cmp_ge_i32_e64 s[62:63], v16, s76
	v_cmp_ge_i32_e64 s[64:65], v17, s76
	v_mov_b32_e32 v139, s26
	v_mbcnt_lo_u32_b32 v139, s58, v139
	v_mbcnt_hi_u32_b32 v139, s59, v139
	v_mbcnt_lo_u32_b32 v139, s60, v139
	v_mbcnt_hi_u32_b32 v139, s61, v139
	v_mbcnt_lo_u32_b32 v139, s62, v139
	v_mbcnt_hi_u32_b32 v139, s63, v139
	v_mbcnt_lo_u32_b32 v139, s64, v139
	v_mbcnt_hi_u32_b32 v139, s65, v139
	v_lshlrev_b32_e32 v139, 2, v139
	s_mov_b64 exec, s[58:59]
	v_add_u32_e32 v142, 0x300, v141
	global_store_dword v139, v142, s[40:41]
	v_add_u32_e32 v139, 4, v139
	s_mov_b64 exec, s[60:61]
	v_add_u32_e32 v143, 0x301, v141
	global_store_dword v139, v143, s[40:41]
	v_add_u32_e32 v139, 4, v139
	s_mov_b64 exec, s[62:63]
	v_add_u32_e32 v144, 0x302, v141
	global_store_dword v139, v144, s[40:41]
	v_add_u32_e32 v139, 4, v139
	s_mov_b64 exec, s[64:65]
	v_add_u32_e32 v145, 0x303, v141
	global_store_dword v139, v145, s[40:41]
	v_add_u32_e32 v139, 4, v139
	s_mov_b64 exec, -1
	s_bcnt1_i32_b64 s4, s[58:59]
	s_add_i32 s26, s26, s4
	s_bcnt1_i32_b64 s4, s[60:61]
	s_add_i32 s26, s26, s4
	s_bcnt1_i32_b64 s4, s[62:63]
	s_add_i32 s26, s26, s4
	s_bcnt1_i32_b64 s4, s[64:65]
	s_add_i32 s26, s26, s4
	s_cmp_le_u32 s79, 4
	s_cbranch_scc1 .Lsel_fsp_bend
	v_cmp_ge_i32_e64 s[58:59], v18, s76
	v_cmp_ge_i32_e64 s[60:61], v19, s76
	v_cmp_ge_i32_e64 s[62:63], v20, s76
	v_cmp_ge_i32_e64 s[64:65], v21, s76
	v_mov_b32_e32 v139, s26
	v_mbcnt_lo_u32_b32 v139, s58, v139
	v_mbcnt_hi_u32_b32 v139, s59, v139
	v_mbcnt_lo_u32_b32 v139, s60, v139
	v_mbcnt_hi_u32_b32 v139, s61, v139
	v_mbcnt_lo_u32_b32 v139, s62, v139
	v_mbcnt_hi_u32_b32 v139, s63, v139
	v_mbcnt_lo_u32_b32 v139, s64, v139
	v_mbcnt_hi_u32_b32 v139, s65, v139
	v_lshlrev_b32_e32 v139, 2, v139
	s_mov_b64 exec, s[58:59]
	v_add_u32_e32 v142, 0x400, v141
	global_store_dword v139, v142, s[40:41]
	v_add_u32_e32 v139, 4, v139
	s_mov_b64 exec, s[60:61]
	v_add_u32_e32 v143, 0x401, v141
	global_store_dword v139, v143, s[40:41]
	v_add_u32_e32 v139, 4, v139
	s_mov_b64 exec, s[62:63]
	v_add_u32_e32 v144, 0x402, v141
	global_store_dword v139, v144, s[40:41]
	v_add_u32_e32 v139, 4, v139
	s_mov_b64 exec, s[64:65]
	v_add_u32_e32 v145, 0x403, v141
	global_store_dword v139, v145, s[40:41]
	v_add_u32_e32 v139, 4, v139
	s_mov_b64 exec, -1
	s_bcnt1_i32_b64 s4, s[58:59]
	s_add_i32 s26, s26, s4
	s_bcnt1_i32_b64 s4, s[60:61]
	s_add_i32 s26, s26, s4
	s_bcnt1_i32_b64 s4, s[62:63]
	s_add_i32 s26, s26, s4
	s_bcnt1_i32_b64 s4, s[64:65]
	s_add_i32 s26, s26, s4
	s_cmp_le_u32 s79, 5
	s_cbranch_scc1 .Lsel_fsp_bend
	v_cmp_ge_i32_e64 s[58:59], v22, s76
	v_cmp_ge_i32_e64 s[60:61], v23, s76
	v_cmp_ge_i32_e64 s[62:63], v24, s76
	v_cmp_ge_i32_e64 s[64:65], v25, s76
	v_mov_b32_e32 v139, s26
	v_mbcnt_lo_u32_b32 v139, s58, v139
	v_mbcnt_hi_u32_b32 v139, s59, v139
	v_mbcnt_lo_u32_b32 v139, s60, v139
	v_mbcnt_hi_u32_b32 v139, s61, v139
	v_mbcnt_lo_u32_b32 v139, s62, v139
	v_mbcnt_hi_u32_b32 v139, s63, v139
	v_mbcnt_lo_u32_b32 v139, s64, v139
	v_mbcnt_hi_u32_b32 v139, s65, v139
	v_lshlrev_b32_e32 v139, 2, v139
	s_mov_b64 exec, s[58:59]
	v_add_u32_e32 v142, 0x500, v141
	global_store_dword v139, v142, s[40:41]
	v_add_u32_e32 v139, 4, v139
	s_mov_b64 exec, s[60:61]
	v_add_u32_e32 v143, 0x501, v141
	global_store_dword v139, v143, s[40:41]
	v_add_u32_e32 v139, 4, v139
	s_mov_b64 exec, s[62:63]
	v_add_u32_e32 v144, 0x502, v141
	global_store_dword v139, v144, s[40:41]
	v_add_u32_e32 v139, 4, v139
	s_mov_b64 exec, s[64:65]
	v_add_u32_e32 v145, 0x503, v141
	global_store_dword v139, v145, s[40:41]
	v_add_u32_e32 v139, 4, v139
	s_mov_b64 exec, -1
	s_bcnt1_i32_b64 s4, s[58:59]
	s_add_i32 s26, s26, s4
	s_bcnt1_i32_b64 s4, s[60:61]
	s_add_i32 s26, s26, s4
	s_bcnt1_i32_b64 s4, s[62:63]
	s_add_i32 s26, s26, s4
	s_bcnt1_i32_b64 s4, s[64:65]
	s_add_i32 s26, s26, s4
	s_cmp_le_u32 s79, 6
	s_cbranch_scc1 .Lsel_fsp_bend
	v_cmp_ge_i32_e64 s[58:59], v26, s76
	v_cmp_ge_i32_e64 s[60:61], v27, s76
	v_cmp_ge_i32_e64 s[62:63], v28, s76
	v_cmp_ge_i32_e64 s[64:65], v29, s76
	v_mov_b32_e32 v139, s26
	v_mbcnt_lo_u32_b32 v139, s58, v139
	v_mbcnt_hi_u32_b32 v139, s59, v139
	v_mbcnt_lo_u32_b32 v139, s60, v139
	v_mbcnt_hi_u32_b32 v139, s61, v139
	v_mbcnt_lo_u32_b32 v139, s62, v139
	v_mbcnt_hi_u32_b32 v139, s63, v139
	v_mbcnt_lo_u32_b32 v139, s64, v139
	v_mbcnt_hi_u32_b32 v139, s65, v139
	v_lshlrev_b32_e32 v139, 2, v139
	s_mov_b64 exec, s[58:59]
	v_add_u32_e32 v142, 0x600, v141
	global_store_dword v139, v142, s[40:41]
	v_add_u32_e32 v139, 4, v139
	s_mov_b64 exec, s[60:61]
	v_add_u32_e32 v143, 0x601, v141
	global_store_dword v139, v143, s[40:41]
	v_add_u32_e32 v139, 4, v139
	s_mov_b64 exec, s[62:63]
	v_add_u32_e32 v144, 0x602, v141
	global_store_dword v139, v144, s[40:41]
	v_add_u32_e32 v139, 4, v139
	s_mov_b64 exec, s[64:65]
	v_add_u32_e32 v145, 0x603, v141
	global_store_dword v139, v145, s[40:41]
	v_add_u32_e32 v139, 4, v139
	s_mov_b64 exec, -1
	s_bcnt1_i32_b64 s4, s[58:59]
	s_add_i32 s26, s26, s4
	s_bcnt1_i32_b64 s4, s[60:61]
	s_add_i32 s26, s26, s4
	s_bcnt1_i32_b64 s4, s[62:63]
	s_add_i32 s26, s26, s4
	s_bcnt1_i32_b64 s4, s[64:65]
	s_add_i32 s26, s26, s4
	s_cmp_le_u32 s79, 7
	s_cbranch_scc1 .Lsel_fsp_bend
	v_cmp_ge_i32_e64 s[58:59], v30, s76
	v_cmp_ge_i32_e64 s[60:61], v31, s76
	v_cmp_ge_i32_e64 s[62:63], v32, s76
	v_cmp_ge_i32_e64 s[64:65], v33, s76
	v_mov_b32_e32 v139, s26
	v_mbcnt_lo_u32_b32 v139, s58, v139
	v_mbcnt_hi_u32_b32 v139, s59, v139
	v_mbcnt_lo_u32_b32 v139, s60, v139
	v_mbcnt_hi_u32_b32 v139, s61, v139
	v_mbcnt_lo_u32_b32 v139, s62, v139
	v_mbcnt_hi_u32_b32 v139, s63, v139
	v_mbcnt_lo_u32_b32 v139, s64, v139
	v_mbcnt_hi_u32_b32 v139, s65, v139
	v_lshlrev_b32_e32 v139, 2, v139
	s_mov_b64 exec, s[58:59]
	v_add_u32_e32 v142, 0x700, v141
	global_store_dword v139, v142, s[40:41]
	v_add_u32_e32 v139, 4, v139
	s_mov_b64 exec, s[60:61]
	v_add_u32_e32 v143, 0x701, v141
	global_store_dword v139, v143, s[40:41]
	v_add_u32_e32 v139, 4, v139
	s_mov_b64 exec, s[62:63]
	v_add_u32_e32 v144, 0x702, v141
	global_store_dword v139, v144, s[40:41]
	v_add_u32_e32 v139, 4, v139
	s_mov_b64 exec, s[64:65]
	v_add_u32_e32 v145, 0x703, v141
	global_store_dword v139, v145, s[40:41]
	v_add_u32_e32 v139, 4, v139
	s_mov_b64 exec, -1
	s_bcnt1_i32_b64 s4, s[58:59]
	s_add_i32 s26, s26, s4
	s_bcnt1_i32_b64 s4, s[60:61]
	s_add_i32 s26, s26, s4
	s_bcnt1_i32_b64 s4, s[62:63]
	s_add_i32 s26, s26, s4
	s_bcnt1_i32_b64 s4, s[64:65]
	s_add_i32 s26, s26, s4
	s_cmp_le_u32 s79, 8
	s_cbranch_scc1 .Lsel_fsp_bend
	v_cmp_ge_i32_e64 s[58:59], v34, s76
	v_cmp_ge_i32_e64 s[60:61], v35, s76
	v_cmp_ge_i32_e64 s[62:63], v36, s76
	v_cmp_ge_i32_e64 s[64:65], v37, s76
	v_mov_b32_e32 v139, s26
	v_mbcnt_lo_u32_b32 v139, s58, v139
	v_mbcnt_hi_u32_b32 v139, s59, v139
	v_mbcnt_lo_u32_b32 v139, s60, v139
	v_mbcnt_hi_u32_b32 v139, s61, v139
	v_mbcnt_lo_u32_b32 v139, s62, v139
	v_mbcnt_hi_u32_b32 v139, s63, v139
	v_mbcnt_lo_u32_b32 v139, s64, v139
	v_mbcnt_hi_u32_b32 v139, s65, v139
	v_lshlrev_b32_e32 v139, 2, v139
	s_mov_b64 exec, s[58:59]
	v_add_u32_e32 v142, 0x800, v141
	global_store_dword v139, v142, s[40:41]
	v_add_u32_e32 v139, 4, v139
	s_mov_b64 exec, s[60:61]
	v_add_u32_e32 v143, 0x801, v141
	global_store_dword v139, v143, s[40:41]
	v_add_u32_e32 v139, 4, v139
	s_mov_b64 exec, s[62:63]
	v_add_u32_e32 v144, 0x802, v141
	global_store_dword v139, v144, s[40:41]
	v_add_u32_e32 v139, 4, v139
	s_mov_b64 exec, s[64:65]
	v_add_u32_e32 v145, 0x803, v141
	global_store_dword v139, v145, s[40:41]
	v_add_u32_e32 v139, 4, v139
	s_mov_b64 exec, -1
	s_bcnt1_i32_b64 s4, s[58:59]
	s_add_i32 s26, s26, s4
	s_bcnt1_i32_b64 s4, s[60:61]
	s_add_i32 s26, s26, s4
	s_bcnt1_i32_b64 s4, s[62:63]
	s_add_i32 s26, s26, s4
	s_bcnt1_i32_b64 s4, s[64:65]
	s_add_i32 s26, s26, s4
	s_cmp_le_u32 s79, 9
	s_cbranch_scc1 .Lsel_fsp_bend
	v_cmp_ge_i32_e64 s[58:59], v38, s76
	v_cmp_ge_i32_e64 s[60:61], v39, s76
	v_cmp_ge_i32_e64 s[62:63], v40, s76
	v_cmp_ge_i32_e64 s[64:65], v41, s76
	v_mov_b32_e32 v139, s26
	v_mbcnt_lo_u32_b32 v139, s58, v139
	v_mbcnt_hi_u32_b32 v139, s59, v139
	v_mbcnt_lo_u32_b32 v139, s60, v139
	v_mbcnt_hi_u32_b32 v139, s61, v139
	v_mbcnt_lo_u32_b32 v139, s62, v139
	v_mbcnt_hi_u32_b32 v139, s63, v139
	v_mbcnt_lo_u32_b32 v139, s64, v139
	v_mbcnt_hi_u32_b32 v139, s65, v139
	v_lshlrev_b32_e32 v139, 2, v139
	s_mov_b64 exec, s[58:59]
	v_add_u32_e32 v142, 0x900, v141
	global_store_dword v139, v142, s[40:41]
	v_add_u32_e32 v139, 4, v139
	s_mov_b64 exec, s[60:61]
	v_add_u32_e32 v143, 0x901, v141
	global_store_dword v139, v143, s[40:41]
	v_add_u32_e32 v139, 4, v139
	s_mov_b64 exec, s[62:63]
	v_add_u32_e32 v144, 0x902, v141
	global_store_dword v139, v144, s[40:41]
	v_add_u32_e32 v139, 4, v139
	s_mov_b64 exec, s[64:65]
	v_add_u32_e32 v145, 0x903, v141
	global_store_dword v139, v145, s[40:41]
	v_add_u32_e32 v139, 4, v139
	s_mov_b64 exec, -1
	s_bcnt1_i32_b64 s4, s[58:59]
	s_add_i32 s26, s26, s4
	s_bcnt1_i32_b64 s4, s[60:61]
	s_add_i32 s26, s26, s4
	s_bcnt1_i32_b64 s4, s[62:63]
	s_add_i32 s26, s26, s4
	s_bcnt1_i32_b64 s4, s[64:65]
	s_add_i32 s26, s26, s4
	s_cmp_le_u32 s79, 10
	s_cbranch_scc1 .Lsel_fsp_bend
	v_cmp_ge_i32_e64 s[58:59], v42, s76
	v_cmp_ge_i32_e64 s[60:61], v43, s76
	v_cmp_ge_i32_e64 s[62:63], v44, s76
	v_cmp_ge_i32_e64 s[64:65], v45, s76
	v_mov_b32_e32 v139, s26
	v_mbcnt_lo_u32_b32 v139, s58, v139
	v_mbcnt_hi_u32_b32 v139, s59, v139
	v_mbcnt_lo_u32_b32 v139, s60, v139
	v_mbcnt_hi_u32_b32 v139, s61, v139
	v_mbcnt_lo_u32_b32 v139, s62, v139
	v_mbcnt_hi_u32_b32 v139, s63, v139
	v_mbcnt_lo_u32_b32 v139, s64, v139
	v_mbcnt_hi_u32_b32 v139, s65, v139
	v_lshlrev_b32_e32 v139, 2, v139
	s_mov_b64 exec, s[58:59]
	v_add_u32_e32 v142, 0xa00, v141
	global_store_dword v139, v142, s[40:41]
	v_add_u32_e32 v139, 4, v139
	s_mov_b64 exec, s[60:61]
	v_add_u32_e32 v143, 0xa01, v141
	global_store_dword v139, v143, s[40:41]
	v_add_u32_e32 v139, 4, v139
	s_mov_b64 exec, s[62:63]
	v_add_u32_e32 v144, 0xa02, v141
	global_store_dword v139, v144, s[40:41]
	v_add_u32_e32 v139, 4, v139
	s_mov_b64 exec, s[64:65]
	v_add_u32_e32 v145, 0xa03, v141
	global_store_dword v139, v145, s[40:41]
	v_add_u32_e32 v139, 4, v139
	s_mov_b64 exec, -1
	s_bcnt1_i32_b64 s4, s[58:59]
	s_add_i32 s26, s26, s4
	s_bcnt1_i32_b64 s4, s[60:61]
	s_add_i32 s26, s26, s4
	s_bcnt1_i32_b64 s4, s[62:63]
	s_add_i32 s26, s26, s4
	s_bcnt1_i32_b64 s4, s[64:65]
	s_add_i32 s26, s26, s4
	s_cmp_le_u32 s79, 11
	s_cbranch_scc1 .Lsel_fsp_bend
	v_cmp_ge_i32_e64 s[58:59], v46, s76
	v_cmp_ge_i32_e64 s[60:61], v47, s76
	v_cmp_ge_i32_e64 s[62:63], v48, s76
	v_cmp_ge_i32_e64 s[64:65], v49, s76
	v_mov_b32_e32 v139, s26
	v_mbcnt_lo_u32_b32 v139, s58, v139
	v_mbcnt_hi_u32_b32 v139, s59, v139
	v_mbcnt_lo_u32_b32 v139, s60, v139
	v_mbcnt_hi_u32_b32 v139, s61, v139
	v_mbcnt_lo_u32_b32 v139, s62, v139
	v_mbcnt_hi_u32_b32 v139, s63, v139
	v_mbcnt_lo_u32_b32 v139, s64, v139
	v_mbcnt_hi_u32_b32 v139, s65, v139
	v_lshlrev_b32_e32 v139, 2, v139
	s_mov_b64 exec, s[58:59]
	v_add_u32_e32 v142, 0xb00, v141
	global_store_dword v139, v142, s[40:41]
	v_add_u32_e32 v139, 4, v139
	s_mov_b64 exec, s[60:61]
	v_add_u32_e32 v143, 0xb01, v141
	global_store_dword v139, v143, s[40:41]
	v_add_u32_e32 v139, 4, v139
	s_mov_b64 exec, s[62:63]
	v_add_u32_e32 v144, 0xb02, v141
	global_store_dword v139, v144, s[40:41]
	v_add_u32_e32 v139, 4, v139
	s_mov_b64 exec, s[64:65]
	v_add_u32_e32 v145, 0xb03, v141
	global_store_dword v139, v145, s[40:41]
	v_add_u32_e32 v139, 4, v139
	s_mov_b64 exec, -1
	s_bcnt1_i32_b64 s4, s[58:59]
	s_add_i32 s26, s26, s4
	s_bcnt1_i32_b64 s4, s[60:61]
	s_add_i32 s26, s26, s4
	s_bcnt1_i32_b64 s4, s[62:63]
	s_add_i32 s26, s26, s4
	s_bcnt1_i32_b64 s4, s[64:65]
	s_add_i32 s26, s26, s4
	s_cmp_le_u32 s79, 12
	s_cbranch_scc1 .Lsel_fsp_bend
	v_cmp_ge_i32_e64 s[58:59], v118, s76
	v_cmp_ge_i32_e64 s[60:61], v119, s76
	v_cmp_ge_i32_e64 s[62:63], v120, s76
	v_cmp_ge_i32_e64 s[64:65], v121, s76
	v_mov_b32_e32 v139, s26
	v_mbcnt_lo_u32_b32 v139, s58, v139
	v_mbcnt_hi_u32_b32 v139, s59, v139
	v_mbcnt_lo_u32_b32 v139, s60, v139
	v_mbcnt_hi_u32_b32 v139, s61, v139
	v_mbcnt_lo_u32_b32 v139, s62, v139
	v_mbcnt_hi_u32_b32 v139, s63, v139
	v_mbcnt_lo_u32_b32 v139, s64, v139
	v_mbcnt_hi_u32_b32 v139, s65, v139
	v_lshlrev_b32_e32 v139, 2, v139
	s_mov_b64 exec, s[58:59]
	v_add_u32_e32 v142, 0xc00, v141
	global_store_dword v139, v142, s[40:41]
	v_add_u32_e32 v139, 4, v139
	s_mov_b64 exec, s[60:61]
	v_add_u32_e32 v143, 0xc01, v141
	global_store_dword v139, v143, s[40:41]
	v_add_u32_e32 v139, 4, v139
	s_mov_b64 exec, s[62:63]
	v_add_u32_e32 v144, 0xc02, v141
	global_store_dword v139, v144, s[40:41]
	v_add_u32_e32 v139, 4, v139
	s_mov_b64 exec, s[64:65]
	v_add_u32_e32 v145, 0xc03, v141
	global_store_dword v139, v145, s[40:41]
	v_add_u32_e32 v139, 4, v139
	s_mov_b64 exec, -1
	s_bcnt1_i32_b64 s4, s[58:59]
	s_add_i32 s26, s26, s4
	s_bcnt1_i32_b64 s4, s[60:61]
	s_add_i32 s26, s26, s4
	s_bcnt1_i32_b64 s4, s[62:63]
	s_add_i32 s26, s26, s4
	s_bcnt1_i32_b64 s4, s[64:65]
	s_add_i32 s26, s26, s4
	s_cmp_le_u32 s79, 13
	s_cbranch_scc1 .Lsel_fsp_bend
	v_cmp_ge_i32_e64 s[58:59], v122, s76
	v_cmp_ge_i32_e64 s[60:61], v123, s76
	v_cmp_ge_i32_e64 s[62:63], v124, s76
	v_cmp_ge_i32_e64 s[64:65], v125, s76
	v_mov_b32_e32 v139, s26
	v_mbcnt_lo_u32_b32 v139, s58, v139
	v_mbcnt_hi_u32_b32 v139, s59, v139
	v_mbcnt_lo_u32_b32 v139, s60, v139
	v_mbcnt_hi_u32_b32 v139, s61, v139
	v_mbcnt_lo_u32_b32 v139, s62, v139
	v_mbcnt_hi_u32_b32 v139, s63, v139
	v_mbcnt_lo_u32_b32 v139, s64, v139
	v_mbcnt_hi_u32_b32 v139, s65, v139
	v_lshlrev_b32_e32 v139, 2, v139
	s_mov_b64 exec, s[58:59]
	v_add_u32_e32 v142, 0xd00, v141
	global_store_dword v139, v142, s[40:41]
	v_add_u32_e32 v139, 4, v139
	s_mov_b64 exec, s[60:61]
	v_add_u32_e32 v143, 0xd01, v141
	global_store_dword v139, v143, s[40:41]
	v_add_u32_e32 v139, 4, v139
	s_mov_b64 exec, s[62:63]
	v_add_u32_e32 v144, 0xd02, v141
	global_store_dword v139, v144, s[40:41]
	v_add_u32_e32 v139, 4, v139
	s_mov_b64 exec, s[64:65]
	v_add_u32_e32 v145, 0xd03, v141
	global_store_dword v139, v145, s[40:41]
	v_add_u32_e32 v139, 4, v139
	s_mov_b64 exec, -1
	s_bcnt1_i32_b64 s4, s[58:59]
	s_add_i32 s26, s26, s4
	s_bcnt1_i32_b64 s4, s[60:61]
	s_add_i32 s26, s26, s4
	s_bcnt1_i32_b64 s4, s[62:63]
	s_add_i32 s26, s26, s4
	s_bcnt1_i32_b64 s4, s[64:65]
	s_add_i32 s26, s26, s4
	s_cmp_le_u32 s79, 14
	s_cbranch_scc1 .Lsel_fsp_bend
	v_cmp_ge_i32_e64 s[58:59], v126, s76
	v_cmp_ge_i32_e64 s[60:61], v127, s76
	v_cmp_ge_i32_e64 s[62:63], v128, s76
	v_cmp_ge_i32_e64 s[64:65], v129, s76
	v_mov_b32_e32 v139, s26
	v_mbcnt_lo_u32_b32 v139, s58, v139
	v_mbcnt_hi_u32_b32 v139, s59, v139
	v_mbcnt_lo_u32_b32 v139, s60, v139
	v_mbcnt_hi_u32_b32 v139, s61, v139
	v_mbcnt_lo_u32_b32 v139, s62, v139
	v_mbcnt_hi_u32_b32 v139, s63, v139
	v_mbcnt_lo_u32_b32 v139, s64, v139
	v_mbcnt_hi_u32_b32 v139, s65, v139
	v_lshlrev_b32_e32 v139, 2, v139
	s_mov_b64 exec, s[58:59]
	v_add_u32_e32 v142, 0xe00, v141
	global_store_dword v139, v142, s[40:41]
	v_add_u32_e32 v139, 4, v139
	s_mov_b64 exec, s[60:61]
	v_add_u32_e32 v143, 0xe01, v141
	global_store_dword v139, v143, s[40:41]
	v_add_u32_e32 v139, 4, v139
	s_mov_b64 exec, s[62:63]
	v_add_u32_e32 v144, 0xe02, v141
	global_store_dword v139, v144, s[40:41]
	v_add_u32_e32 v139, 4, v139
	s_mov_b64 exec, s[64:65]
	v_add_u32_e32 v145, 0xe03, v141
	global_store_dword v139, v145, s[40:41]
	v_add_u32_e32 v139, 4, v139
	s_mov_b64 exec, -1
	s_bcnt1_i32_b64 s4, s[58:59]
	s_add_i32 s26, s26, s4
	s_bcnt1_i32_b64 s4, s[60:61]
	s_add_i32 s26, s26, s4
	s_bcnt1_i32_b64 s4, s[62:63]
	s_add_i32 s26, s26, s4
	s_bcnt1_i32_b64 s4, s[64:65]
	s_add_i32 s26, s26, s4
	s_cmp_le_u32 s79, 15
	s_cbranch_scc1 .Lsel_fsp_bend
	v_cmp_ge_i32_e64 s[58:59], v130, s76
	v_cmp_ge_i32_e64 s[60:61], v131, s76
	v_cmp_ge_i32_e64 s[62:63], v132, s76
	v_cmp_ge_i32_e64 s[64:65], v133, s76
	v_mov_b32_e32 v139, s26
	v_mbcnt_lo_u32_b32 v139, s58, v139
	v_mbcnt_hi_u32_b32 v139, s59, v139
	v_mbcnt_lo_u32_b32 v139, s60, v139
	v_mbcnt_hi_u32_b32 v139, s61, v139
	v_mbcnt_lo_u32_b32 v139, s62, v139
	v_mbcnt_hi_u32_b32 v139, s63, v139
	v_mbcnt_lo_u32_b32 v139, s64, v139
	v_mbcnt_hi_u32_b32 v139, s65, v139
	v_lshlrev_b32_e32 v139, 2, v139
	s_mov_b64 exec, s[58:59]
	v_add_u32_e32 v142, 0xf00, v141
	global_store_dword v139, v142, s[40:41]
	v_add_u32_e32 v139, 4, v139
	s_mov_b64 exec, s[60:61]
	v_add_u32_e32 v143, 0xf01, v141
	global_store_dword v139, v143, s[40:41]
	v_add_u32_e32 v139, 4, v139
	s_mov_b64 exec, s[62:63]
	v_add_u32_e32 v144, 0xf02, v141
	global_store_dword v139, v144, s[40:41]
	v_add_u32_e32 v139, 4, v139
	s_mov_b64 exec, s[64:65]
	v_add_u32_e32 v145, 0xf03, v141
	global_store_dword v139, v145, s[40:41]
	v_add_u32_e32 v139, 4, v139
	s_mov_b64 exec, -1
	s_bcnt1_i32_b64 s4, s[58:59]
	s_add_i32 s26, s26, s4
	s_bcnt1_i32_b64 s4, s[60:61]
	s_add_i32 s26, s26, s4
	s_bcnt1_i32_b64 s4, s[62:63]
	s_add_i32 s26, s26, s4
	s_bcnt1_i32_b64 s4, s[64:65]
	s_add_i32 s26, s26, s4

.Lsel_ld11_end:
.Lsel_fsn_nonext:
	v_add_u32_e32 v141, s16, v56
	v_cmp_le_u32_e64 s[58:59], v2, s76
	v_cmp_le_u32_e64 s[60:61], v3, s76
	v_cmp_le_u32_e64 s[62:63], v4, s76
	v_cmp_le_u32_e64 s[64:65], v5, s76
	v_mov_b32_e32 v139, s26
	v_mbcnt_lo_u32_b32 v139, s58, v139
	v_mbcnt_hi_u32_b32 v139, s59, v139
	v_mbcnt_lo_u32_b32 v139, s60, v139
	v_mbcnt_hi_u32_b32 v139, s61, v139
	v_mbcnt_lo_u32_b32 v139, s62, v139
	v_mbcnt_hi_u32_b32 v139, s63, v139
	v_mbcnt_lo_u32_b32 v139, s64, v139
	v_mbcnt_hi_u32_b32 v139, s65, v139
	v_lshlrev_b32_e32 v139, 2, v139
	s_mov_b64 exec, s[58:59]
	v_add_u32_e32 v142, 0, v141
	global_store_dword v139, v142, s[40:41]
	v_add_u32_e32 v139, 4, v139
	s_mov_b64 exec, s[60:61]
	v_add_u32_e32 v143, 1, v141
	global_store_dword v139, v143, s[40:41]
	v_add_u32_e32 v139, 4, v139
	s_mov_b64 exec, s[62:63]
	v_add_u32_e32 v144, 2, v141
	global_store_dword v139, v144, s[40:41]
	v_add_u32_e32 v139, 4, v139
	s_mov_b64 exec, s[64:65]
	v_add_u32_e32 v145, 3, v141
	global_store_dword v139, v145, s[40:41]
	v_add_u32_e32 v139, 4, v139
	s_mov_b64 exec, -1
	s_bcnt1_i32_b64 s4, s[58:59]
	s_add_i32 s26, s26, s4
	s_bcnt1_i32_b64 s4, s[60:61]
	s_add_i32 s26, s26, s4
	s_bcnt1_i32_b64 s4, s[62:63]
	s_add_i32 s26, s26, s4
	s_bcnt1_i32_b64 s4, s[64:65]
	s_add_i32 s26, s26, s4
	s_cmp_le_u32 s79, 1
	s_cbranch_scc1 .Lsel_fsn_bend
	v_cmp_le_u32_e64 s[58:59], v6, s76
	v_cmp_le_u32_e64 s[60:61], v7, s76
	v_cmp_le_u32_e64 s[62:63], v8, s76
	v_cmp_le_u32_e64 s[64:65], v9, s76
	v_mov_b32_e32 v139, s26
	v_mbcnt_lo_u32_b32 v139, s58, v139
	v_mbcnt_hi_u32_b32 v139, s59, v139
	v_mbcnt_lo_u32_b32 v139, s60, v139
	v_mbcnt_hi_u32_b32 v139, s61, v139
	v_mbcnt_lo_u32_b32 v139, s62, v139
	v_mbcnt_hi_u32_b32 v139, s63, v139
	v_mbcnt_lo_u32_b32 v139, s64, v139
	v_mbcnt_hi_u32_b32 v139, s65, v139
	v_lshlrev_b32_e32 v139, 2, v139
	s_mov_b64 exec, s[58:59]
	v_add_u32_e32 v142, 0x100, v141
	global_store_dword v139, v142, s[40:41]
	v_add_u32_e32 v139, 4, v139
	s_mov_b64 exec, s[60:61]
	v_add_u32_e32 v143, 0x101, v141
	global_store_dword v139, v143, s[40:41]
	v_add_u32_e32 v139, 4, v139
	s_mov_b64 exec, s[62:63]
	v_add_u32_e32 v144, 0x102, v141
	global_store_dword v139, v144, s[40:41]
	v_add_u32_e32 v139, 4, v139
	s_mov_b64 exec, s[64:65]
	v_add_u32_e32 v145, 0x103, v141
	global_store_dword v139, v145, s[40:41]
	v_add_u32_e32 v139, 4, v139
	s_mov_b64 exec, -1
	s_bcnt1_i32_b64 s4, s[58:59]
	s_add_i32 s26, s26, s4
	s_bcnt1_i32_b64 s4, s[60:61]
	s_add_i32 s26, s26, s4
	s_bcnt1_i32_b64 s4, s[62:63]
	s_add_i32 s26, s26, s4
	s_bcnt1_i32_b64 s4, s[64:65]
	s_add_i32 s26, s26, s4
	s_cmp_le_u32 s79, 2
	s_cbranch_scc1 .Lsel_fsn_bend
	v_cmp_le_u32_e64 s[58:59], v10, s76
	v_cmp_le_u32_e64 s[60:61], v11, s76
	v_cmp_le_u32_e64 s[62:63], v12, s76
	v_cmp_le_u32_e64 s[64:65], v13, s76
	v_mov_b32_e32 v139, s26
	v_mbcnt_lo_u32_b32 v139, s58, v139
	v_mbcnt_hi_u32_b32 v139, s59, v139
	v_mbcnt_lo_u32_b32 v139, s60, v139
	v_mbcnt_hi_u32_b32 v139, s61, v139
	v_mbcnt_lo_u32_b32 v139, s62, v139
	v_mbcnt_hi_u32_b32 v139, s63, v139
	v_mbcnt_lo_u32_b32 v139, s64, v139
	v_mbcnt_hi_u32_b32 v139, s65, v139
	v_lshlrev_b32_e32 v139, 2, v139
	s_mov_b64 exec, s[58:59]
	v_add_u32_e32 v142, 0x200, v141
	global_store_dword v139, v142, s[40:41]
	v_add_u32_e32 v139, 4, v139
	s_mov_b64 exec, s[60:61]
	v_add_u32_e32 v143, 0x201, v141
	global_store_dword v139, v143, s[40:41]
	v_add_u32_e32 v139, 4, v139
	s_mov_b64 exec, s[62:63]
	v_add_u32_e32 v144, 0x202, v141
	global_store_dword v139, v144, s[40:41]
	v_add_u32_e32 v139, 4, v139
	s_mov_b64 exec, s[64:65]
	v_add_u32_e32 v145, 0x203, v141
	global_store_dword v139, v145, s[40:41]
	v_add_u32_e32 v139, 4, v139
	s_mov_b64 exec, -1
	s_bcnt1_i32_b64 s4, s[58:59]
	s_add_i32 s26, s26, s4
	s_bcnt1_i32_b64 s4, s[60:61]
	s_add_i32 s26, s26, s4
	s_bcnt1_i32_b64 s4, s[62:63]
	s_add_i32 s26, s26, s4
	s_bcnt1_i32_b64 s4, s[64:65]
	s_add_i32 s26, s26, s4
	s_cmp_le_u32 s79, 3
	s_cbranch_scc1 .Lsel_fsn_bend
	v_cmp_le_u32_e64 s[58:59], v14, s76
	v_cmp_le_u32_e64 s[60:61], v15, s76
	v_cmp_le_u32_e64 s[62:63], v16, s76
	v_cmp_le_u32_e64 s[64:65], v17, s76
	v_mov_b32_e32 v139, s26
	v_mbcnt_lo_u32_b32 v139, s58, v139
	v_mbcnt_hi_u32_b32 v139, s59, v139
	v_mbcnt_lo_u32_b32 v139, s60, v139
	v_mbcnt_hi_u32_b32 v139, s61, v139
	v_mbcnt_lo_u32_b32 v139, s62, v139
	v_mbcnt_hi_u32_b32 v139, s63, v139
	v_mbcnt_lo_u32_b32 v139, s64, v139
	v_mbcnt_hi_u32_b32 v139, s65, v139
	v_lshlrev_b32_e32 v139, 2, v139
	s_mov_b64 exec, s[58:59]
	v_add_u32_e32 v142, 0x300, v141
	global_store_dword v139, v142, s[40:41]
	v_add_u32_e32 v139, 4, v139
	s_mov_b64 exec, s[60:61]
	v_add_u32_e32 v143, 0x301, v141
	global_store_dword v139, v143, s[40:41]
	v_add_u32_e32 v139, 4, v139
	s_mov_b64 exec, s[62:63]
	v_add_u32_e32 v144, 0x302, v141
	global_store_dword v139, v144, s[40:41]
	v_add_u32_e32 v139, 4, v139
	s_mov_b64 exec, s[64:65]
	v_add_u32_e32 v145, 0x303, v141
	global_store_dword v139, v145, s[40:41]
	v_add_u32_e32 v139, 4, v139
	s_mov_b64 exec, -1
	s_bcnt1_i32_b64 s4, s[58:59]
	s_add_i32 s26, s26, s4
	s_bcnt1_i32_b64 s4, s[60:61]
	s_add_i32 s26, s26, s4
	s_bcnt1_i32_b64 s4, s[62:63]
	s_add_i32 s26, s26, s4
	s_bcnt1_i32_b64 s4, s[64:65]
	s_add_i32 s26, s26, s4
	s_cmp_le_u32 s79, 4
	s_cbranch_scc1 .Lsel_fsn_bend
	v_cmp_le_u32_e64 s[58:59], v18, s76
	v_cmp_le_u32_e64 s[60:61], v19, s76
	v_cmp_le_u32_e64 s[62:63], v20, s76
	v_cmp_le_u32_e64 s[64:65], v21, s76
	v_mov_b32_e32 v139, s26
	v_mbcnt_lo_u32_b32 v139, s58, v139
	v_mbcnt_hi_u32_b32 v139, s59, v139
	v_mbcnt_lo_u32_b32 v139, s60, v139
	v_mbcnt_hi_u32_b32 v139, s61, v139
	v_mbcnt_lo_u32_b32 v139, s62, v139
	v_mbcnt_hi_u32_b32 v139, s63, v139
	v_mbcnt_lo_u32_b32 v139, s64, v139
	v_mbcnt_hi_u32_b32 v139, s65, v139
	v_lshlrev_b32_e32 v139, 2, v139
	s_mov_b64 exec, s[58:59]
	v_add_u32_e32 v142, 0x400, v141
	global_store_dword v139, v142, s[40:41]
	v_add_u32_e32 v139, 4, v139
	s_mov_b64 exec, s[60:61]
	v_add_u32_e32 v143, 0x401, v141
	global_store_dword v139, v143, s[40:41]
	v_add_u32_e32 v139, 4, v139
	s_mov_b64 exec, s[62:63]
	v_add_u32_e32 v144, 0x402, v141
	global_store_dword v139, v144, s[40:41]
	v_add_u32_e32 v139, 4, v139
	s_mov_b64 exec, s[64:65]
	v_add_u32_e32 v145, 0x403, v141
	global_store_dword v139, v145, s[40:41]
	v_add_u32_e32 v139, 4, v139
	s_mov_b64 exec, -1
	s_bcnt1_i32_b64 s4, s[58:59]
	s_add_i32 s26, s26, s4
	s_bcnt1_i32_b64 s4, s[60:61]
	s_add_i32 s26, s26, s4
	s_bcnt1_i32_b64 s4, s[62:63]
	s_add_i32 s26, s26, s4
	s_bcnt1_i32_b64 s4, s[64:65]
	s_add_i32 s26, s26, s4
	s_cmp_le_u32 s79, 5
	s_cbranch_scc1 .Lsel_fsn_bend
	v_cmp_le_u32_e64 s[58:59], v22, s76
	v_cmp_le_u32_e64 s[60:61], v23, s76
	v_cmp_le_u32_e64 s[62:63], v24, s76
	v_cmp_le_u32_e64 s[64:65], v25, s76
	v_mov_b32_e32 v139, s26
	v_mbcnt_lo_u32_b32 v139, s58, v139
	v_mbcnt_hi_u32_b32 v139, s59, v139
	v_mbcnt_lo_u32_b32 v139, s60, v139
	v_mbcnt_hi_u32_b32 v139, s61, v139
	v_mbcnt_lo_u32_b32 v139, s62, v139
	v_mbcnt_hi_u32_b32 v139, s63, v139
	v_mbcnt_lo_u32_b32 v139, s64, v139
	v_mbcnt_hi_u32_b32 v139, s65, v139
	v_lshlrev_b32_e32 v139, 2, v139
	s_mov_b64 exec, s[58:59]
	v_add_u32_e32 v142, 0x500, v141
	global_store_dword v139, v142, s[40:41]
	v_add_u32_e32 v139, 4, v139
	s_mov_b64 exec, s[60:61]
	v_add_u32_e32 v143, 0x501, v141
	global_store_dword v139, v143, s[40:41]
	v_add_u32_e32 v139, 4, v139
	s_mov_b64 exec, s[62:63]
	v_add_u32_e32 v144, 0x502, v141
	global_store_dword v139, v144, s[40:41]
	v_add_u32_e32 v139, 4, v139
	s_mov_b64 exec, s[64:65]
	v_add_u32_e32 v145, 0x503, v141
	global_store_dword v139, v145, s[40:41]
	v_add_u32_e32 v139, 4, v139
	s_mov_b64 exec, -1
	s_bcnt1_i32_b64 s4, s[58:59]
	s_add_i32 s26, s26, s4
	s_bcnt1_i32_b64 s4, s[60:61]
	s_add_i32 s26, s26, s4
	s_bcnt1_i32_b64 s4, s[62:63]
	s_add_i32 s26, s26, s4
	s_bcnt1_i32_b64 s4, s[64:65]
	s_add_i32 s26, s26, s4
	s_cmp_le_u32 s79, 6
	s_cbranch_scc1 .Lsel_fsn_bend
	v_cmp_le_u32_e64 s[58:59], v26, s76
	v_cmp_le_u32_e64 s[60:61], v27, s76
	v_cmp_le_u32_e64 s[62:63], v28, s76
	v_cmp_le_u32_e64 s[64:65], v29, s76
	v_mov_b32_e32 v139, s26
	v_mbcnt_lo_u32_b32 v139, s58, v139
	v_mbcnt_hi_u32_b32 v139, s59, v139
	v_mbcnt_lo_u32_b32 v139, s60, v139
	v_mbcnt_hi_u32_b32 v139, s61, v139
	v_mbcnt_lo_u32_b32 v139, s62, v139
	v_mbcnt_hi_u32_b32 v139, s63, v139
	v_mbcnt_lo_u32_b32 v139, s64, v139
	v_mbcnt_hi_u32_b32 v139, s65, v139
	v_lshlrev_b32_e32 v139, 2, v139
	s_mov_b64 exec, s[58:59]
	v_add_u32_e32 v142, 0x600, v141
	global_store_dword v139, v142, s[40:41]
	v_add_u32_e32 v139, 4, v139
	s_mov_b64 exec, s[60:61]
	v_add_u32_e32 v143, 0x601, v141
	global_store_dword v139, v143, s[40:41]
	v_add_u32_e32 v139, 4, v139
	s_mov_b64 exec, s[62:63]
	v_add_u32_e32 v144, 0x602, v141
	global_store_dword v139, v144, s[40:41]
	v_add_u32_e32 v139, 4, v139
	s_mov_b64 exec, s[64:65]
	v_add_u32_e32 v145, 0x603, v141
	global_store_dword v139, v145, s[40:41]
	v_add_u32_e32 v139, 4, v139
	s_mov_b64 exec, -1
	s_bcnt1_i32_b64 s4, s[58:59]
	s_add_i32 s26, s26, s4
	s_bcnt1_i32_b64 s4, s[60:61]
	s_add_i32 s26, s26, s4
	s_bcnt1_i32_b64 s4, s[62:63]
	s_add_i32 s26, s26, s4
	s_bcnt1_i32_b64 s4, s[64:65]
	s_add_i32 s26, s26, s4
	s_cmp_le_u32 s79, 7
	s_cbranch_scc1 .Lsel_fsn_bend
	v_cmp_le_u32_e64 s[58:59], v30, s76
	v_cmp_le_u32_e64 s[60:61], v31, s76
	v_cmp_le_u32_e64 s[62:63], v32, s76
	v_cmp_le_u32_e64 s[64:65], v33, s76
	v_mov_b32_e32 v139, s26
	v_mbcnt_lo_u32_b32 v139, s58, v139
	v_mbcnt_hi_u32_b32 v139, s59, v139
	v_mbcnt_lo_u32_b32 v139, s60, v139
	v_mbcnt_hi_u32_b32 v139, s61, v139
	v_mbcnt_lo_u32_b32 v139, s62, v139
	v_mbcnt_hi_u32_b32 v139, s63, v139
	v_mbcnt_lo_u32_b32 v139, s64, v139
	v_mbcnt_hi_u32_b32 v139, s65, v139
	v_lshlrev_b32_e32 v139, 2, v139
	s_mov_b64 exec, s[58:59]
	v_add_u32_e32 v142, 0x700, v141
	global_store_dword v139, v142, s[40:41]
	v_add_u32_e32 v139, 4, v139
	s_mov_b64 exec, s[60:61]
	v_add_u32_e32 v143, 0x701, v141
	global_store_dword v139, v143, s[40:41]
	v_add_u32_e32 v139, 4, v139
	s_mov_b64 exec, s[62:63]
	v_add_u32_e32 v144, 0x702, v141
	global_store_dword v139, v144, s[40:41]
	v_add_u32_e32 v139, 4, v139
	s_mov_b64 exec, s[64:65]
	v_add_u32_e32 v145, 0x703, v141
	global_store_dword v139, v145, s[40:41]
	v_add_u32_e32 v139, 4, v139
	s_mov_b64 exec, -1
	s_bcnt1_i32_b64 s4, s[58:59]
	s_add_i32 s26, s26, s4
	s_bcnt1_i32_b64 s4, s[60:61]
	s_add_i32 s26, s26, s4
	s_bcnt1_i32_b64 s4, s[62:63]
	s_add_i32 s26, s26, s4
	s_bcnt1_i32_b64 s4, s[64:65]
	s_add_i32 s26, s26, s4
	s_cmp_le_u32 s79, 8
	s_cbranch_scc1 .Lsel_fsn_bend
	v_cmp_le_u32_e64 s[58:59], v34, s76
	v_cmp_le_u32_e64 s[60:61], v35, s76
	v_cmp_le_u32_e64 s[62:63], v36, s76
	v_cmp_le_u32_e64 s[64:65], v37, s76
	v_mov_b32_e32 v139, s26
	v_mbcnt_lo_u32_b32 v139, s58, v139
	v_mbcnt_hi_u32_b32 v139, s59, v139
	v_mbcnt_lo_u32_b32 v139, s60, v139
	v_mbcnt_hi_u32_b32 v139, s61, v139
	v_mbcnt_lo_u32_b32 v139, s62, v139
	v_mbcnt_hi_u32_b32 v139, s63, v139
	v_mbcnt_lo_u32_b32 v139, s64, v139
	v_mbcnt_hi_u32_b32 v139, s65, v139
	v_lshlrev_b32_e32 v139, 2, v139
	s_mov_b64 exec, s[58:59]
	v_add_u32_e32 v142, 0x800, v141
	global_store_dword v139, v142, s[40:41]
	v_add_u32_e32 v139, 4, v139
	s_mov_b64 exec, s[60:61]
	v_add_u32_e32 v143, 0x801, v141
	global_store_dword v139, v143, s[40:41]
	v_add_u32_e32 v139, 4, v139
	s_mov_b64 exec, s[62:63]
	v_add_u32_e32 v144, 0x802, v141
	global_store_dword v139, v144, s[40:41]
	v_add_u32_e32 v139, 4, v139
	s_mov_b64 exec, s[64:65]
	v_add_u32_e32 v145, 0x803, v141
	global_store_dword v139, v145, s[40:41]
	v_add_u32_e32 v139, 4, v139
	s_mov_b64 exec, -1
	s_bcnt1_i32_b64 s4, s[58:59]
	s_add_i32 s26, s26, s4
	s_bcnt1_i32_b64 s4, s[60:61]
	s_add_i32 s26, s26, s4
	s_bcnt1_i32_b64 s4, s[62:63]
	s_add_i32 s26, s26, s4
	s_bcnt1_i32_b64 s4, s[64:65]
	s_add_i32 s26, s26, s4
	s_cmp_le_u32 s79, 9
	s_cbranch_scc1 .Lsel_fsn_bend
	v_cmp_le_u32_e64 s[58:59], v38, s76
	v_cmp_le_u32_e64 s[60:61], v39, s76
	v_cmp_le_u32_e64 s[62:63], v40, s76
	v_cmp_le_u32_e64 s[64:65], v41, s76
	v_mov_b32_e32 v139, s26
	v_mbcnt_lo_u32_b32 v139, s58, v139
	v_mbcnt_hi_u32_b32 v139, s59, v139
	v_mbcnt_lo_u32_b32 v139, s60, v139
	v_mbcnt_hi_u32_b32 v139, s61, v139
	v_mbcnt_lo_u32_b32 v139, s62, v139
	v_mbcnt_hi_u32_b32 v139, s63, v139
	v_mbcnt_lo_u32_b32 v139, s64, v139
	v_mbcnt_hi_u32_b32 v139, s65, v139
	v_lshlrev_b32_e32 v139, 2, v139
	s_mov_b64 exec, s[58:59]
	v_add_u32_e32 v142, 0x900, v141
	global_store_dword v139, v142, s[40:41]
	v_add_u32_e32 v139, 4, v139
	s_mov_b64 exec, s[60:61]
	v_add_u32_e32 v143, 0x901, v141
	global_store_dword v139, v143, s[40:41]
	v_add_u32_e32 v139, 4, v139
	s_mov_b64 exec, s[62:63]
	v_add_u32_e32 v144, 0x902, v141
	global_store_dword v139, v144, s[40:41]
	v_add_u32_e32 v139, 4, v139
	s_mov_b64 exec, s[64:65]
	v_add_u32_e32 v145, 0x903, v141
	global_store_dword v139, v145, s[40:41]
	v_add_u32_e32 v139, 4, v139
	s_mov_b64 exec, -1
	s_bcnt1_i32_b64 s4, s[58:59]
	s_add_i32 s26, s26, s4
	s_bcnt1_i32_b64 s4, s[60:61]
	s_add_i32 s26, s26, s4
	s_bcnt1_i32_b64 s4, s[62:63]
	s_add_i32 s26, s26, s4
	s_bcnt1_i32_b64 s4, s[64:65]
	s_add_i32 s26, s26, s4
	s_cmp_le_u32 s79, 10
	s_cbranch_scc1 .Lsel_fsn_bend
	v_cmp_le_u32_e64 s[58:59], v42, s76
	v_cmp_le_u32_e64 s[60:61], v43, s76
	v_cmp_le_u32_e64 s[62:63], v44, s76
	v_cmp_le_u32_e64 s[64:65], v45, s76
	v_mov_b32_e32 v139, s26
	v_mbcnt_lo_u32_b32 v139, s58, v139
	v_mbcnt_hi_u32_b32 v139, s59, v139
	v_mbcnt_lo_u32_b32 v139, s60, v139
	v_mbcnt_hi_u32_b32 v139, s61, v139
	v_mbcnt_lo_u32_b32 v139, s62, v139
	v_mbcnt_hi_u32_b32 v139, s63, v139
	v_mbcnt_lo_u32_b32 v139, s64, v139
	v_mbcnt_hi_u32_b32 v139, s65, v139
	v_lshlrev_b32_e32 v139, 2, v139
	s_mov_b64 exec, s[58:59]
	v_add_u32_e32 v142, 0xa00, v141
	global_store_dword v139, v142, s[40:41]
	v_add_u32_e32 v139, 4, v139
	s_mov_b64 exec, s[60:61]
	v_add_u32_e32 v143, 0xa01, v141
	global_store_dword v139, v143, s[40:41]
	v_add_u32_e32 v139, 4, v139
	s_mov_b64 exec, s[62:63]
	v_add_u32_e32 v144, 0xa02, v141
	global_store_dword v139, v144, s[40:41]
	v_add_u32_e32 v139, 4, v139
	s_mov_b64 exec, s[64:65]
	v_add_u32_e32 v145, 0xa03, v141
	global_store_dword v139, v145, s[40:41]
	v_add_u32_e32 v139, 4, v139
	s_mov_b64 exec, -1
	s_bcnt1_i32_b64 s4, s[58:59]
	s_add_i32 s26, s26, s4
	s_bcnt1_i32_b64 s4, s[60:61]
	s_add_i32 s26, s26, s4
	s_bcnt1_i32_b64 s4, s[62:63]
	s_add_i32 s26, s26, s4
	s_bcnt1_i32_b64 s4, s[64:65]
	s_add_i32 s26, s26, s4
	s_cmp_le_u32 s79, 11
	s_cbranch_scc1 .Lsel_fsn_bend
	v_cmp_le_u32_e64 s[58:59], v46, s76
	v_cmp_le_u32_e64 s[60:61], v47, s76
	v_cmp_le_u32_e64 s[62:63], v48, s76
	v_cmp_le_u32_e64 s[64:65], v49, s76
	v_mov_b32_e32 v139, s26
	v_mbcnt_lo_u32_b32 v139, s58, v139
	v_mbcnt_hi_u32_b32 v139, s59, v139
	v_mbcnt_lo_u32_b32 v139, s60, v139
	v_mbcnt_hi_u32_b32 v139, s61, v139
	v_mbcnt_lo_u32_b32 v139, s62, v139
	v_mbcnt_hi_u32_b32 v139, s63, v139
	v_mbcnt_lo_u32_b32 v139, s64, v139
	v_mbcnt_hi_u32_b32 v139, s65, v139
	v_lshlrev_b32_e32 v139, 2, v139
	s_mov_b64 exec, s[58:59]
	v_add_u32_e32 v142, 0xb00, v141
	global_store_dword v139, v142, s[40:41]
	v_add_u32_e32 v139, 4, v139
	s_mov_b64 exec, s[60:61]
	v_add_u32_e32 v143, 0xb01, v141
	global_store_dword v139, v143, s[40:41]
	v_add_u32_e32 v139, 4, v139
	s_mov_b64 exec, s[62:63]
	v_add_u32_e32 v144, 0xb02, v141
	global_store_dword v139, v144, s[40:41]
	v_add_u32_e32 v139, 4, v139
	s_mov_b64 exec, s[64:65]
	v_add_u32_e32 v145, 0xb03, v141
	global_store_dword v139, v145, s[40:41]
	v_add_u32_e32 v139, 4, v139
	s_mov_b64 exec, -1
	s_bcnt1_i32_b64 s4, s[58:59]
	s_add_i32 s26, s26, s4
	s_bcnt1_i32_b64 s4, s[60:61]
	s_add_i32 s26, s26, s4
	s_bcnt1_i32_b64 s4, s[62:63]
	s_add_i32 s26, s26, s4
	s_bcnt1_i32_b64 s4, s[64:65]
	s_add_i32 s26, s26, s4
	s_cmp_le_u32 s79, 12
	s_cbranch_scc1 .Lsel_fsn_bend
	v_cmp_le_u32_e64 s[58:59], v118, s76
	v_cmp_le_u32_e64 s[60:61], v119, s76
	v_cmp_le_u32_e64 s[62:63], v120, s76
	v_cmp_le_u32_e64 s[64:65], v121, s76
	v_mov_b32_e32 v139, s26
	v_mbcnt_lo_u32_b32 v139, s58, v139
	v_mbcnt_hi_u32_b32 v139, s59, v139
	v_mbcnt_lo_u32_b32 v139, s60, v139
	v_mbcnt_hi_u32_b32 v139, s61, v139
	v_mbcnt_lo_u32_b32 v139, s62, v139
	v_mbcnt_hi_u32_b32 v139, s63, v139
	v_mbcnt_lo_u32_b32 v139, s64, v139
	v_mbcnt_hi_u32_b32 v139, s65, v139
	v_lshlrev_b32_e32 v139, 2, v139
	s_mov_b64 exec, s[58:59]
	v_add_u32_e32 v142, 0xc00, v141
	global_store_dword v139, v142, s[40:41]
	v_add_u32_e32 v139, 4, v139
	s_mov_b64 exec, s[60:61]
	v_add_u32_e32 v143, 0xc01, v141
	global_store_dword v139, v143, s[40:41]
	v_add_u32_e32 v139, 4, v139
	s_mov_b64 exec, s[62:63]
	v_add_u32_e32 v144, 0xc02, v141
	global_store_dword v139, v144, s[40:41]
	v_add_u32_e32 v139, 4, v139
	s_mov_b64 exec, s[64:65]
	v_add_u32_e32 v145, 0xc03, v141
	global_store_dword v139, v145, s[40:41]
	v_add_u32_e32 v139, 4, v139
	s_mov_b64 exec, -1
	s_bcnt1_i32_b64 s4, s[58:59]
	s_add_i32 s26, s26, s4
	s_bcnt1_i32_b64 s4, s[60:61]
	s_add_i32 s26, s26, s4
	s_bcnt1_i32_b64 s4, s[62:63]
	s_add_i32 s26, s26, s4
	s_bcnt1_i32_b64 s4, s[64:65]
	s_add_i32 s26, s26, s4
	s_cmp_le_u32 s79, 13
	s_cbranch_scc1 .Lsel_fsn_bend
	v_cmp_le_u32_e64 s[58:59], v122, s76
	v_cmp_le_u32_e64 s[60:61], v123, s76
	v_cmp_le_u32_e64 s[62:63], v124, s76
	v_cmp_le_u32_e64 s[64:65], v125, s76
	v_mov_b32_e32 v139, s26
	v_mbcnt_lo_u32_b32 v139, s58, v139
	v_mbcnt_hi_u32_b32 v139, s59, v139
	v_mbcnt_lo_u32_b32 v139, s60, v139
	v_mbcnt_hi_u32_b32 v139, s61, v139
	v_mbcnt_lo_u32_b32 v139, s62, v139
	v_mbcnt_hi_u32_b32 v139, s63, v139
	v_mbcnt_lo_u32_b32 v139, s64, v139
	v_mbcnt_hi_u32_b32 v139, s65, v139
	v_lshlrev_b32_e32 v139, 2, v139
	s_mov_b64 exec, s[58:59]
	v_add_u32_e32 v142, 0xd00, v141
	global_store_dword v139, v142, s[40:41]
	v_add_u32_e32 v139, 4, v139
	s_mov_b64 exec, s[60:61]
	v_add_u32_e32 v143, 0xd01, v141
	global_store_dword v139, v143, s[40:41]
	v_add_u32_e32 v139, 4, v139
	s_mov_b64 exec, s[62:63]
	v_add_u32_e32 v144, 0xd02, v141
	global_store_dword v139, v144, s[40:41]
	v_add_u32_e32 v139, 4, v139
	s_mov_b64 exec, s[64:65]
	v_add_u32_e32 v145, 0xd03, v141
	global_store_dword v139, v145, s[40:41]
	v_add_u32_e32 v139, 4, v139
	s_mov_b64 exec, -1
	s_bcnt1_i32_b64 s4, s[58:59]
	s_add_i32 s26, s26, s4
	s_bcnt1_i32_b64 s4, s[60:61]
	s_add_i32 s26, s26, s4
	s_bcnt1_i32_b64 s4, s[62:63]
	s_add_i32 s26, s26, s4
	s_bcnt1_i32_b64 s4, s[64:65]
	s_add_i32 s26, s26, s4
	s_cmp_le_u32 s79, 14
	s_cbranch_scc1 .Lsel_fsn_bend
	v_cmp_le_u32_e64 s[58:59], v126, s76
	v_cmp_le_u32_e64 s[60:61], v127, s76
	v_cmp_le_u32_e64 s[62:63], v128, s76
	v_cmp_le_u32_e64 s[64:65], v129, s76
	v_mov_b32_e32 v139, s26
	v_mbcnt_lo_u32_b32 v139, s58, v139
	v_mbcnt_hi_u32_b32 v139, s59, v139
	v_mbcnt_lo_u32_b32 v139, s60, v139
	v_mbcnt_hi_u32_b32 v139, s61, v139
	v_mbcnt_lo_u32_b32 v139, s62, v139
	v_mbcnt_hi_u32_b32 v139, s63, v139
	v_mbcnt_lo_u32_b32 v139, s64, v139
	v_mbcnt_hi_u32_b32 v139, s65, v139
	v_lshlrev_b32_e32 v139, 2, v139
	s_mov_b64 exec, s[58:59]
	v_add_u32_e32 v142, 0xe00, v141
	global_store_dword v139, v142, s[40:41]
	v_add_u32_e32 v139, 4, v139
	s_mov_b64 exec, s[60:61]
	v_add_u32_e32 v143, 0xe01, v141
	global_store_dword v139, v143, s[40:41]
	v_add_u32_e32 v139, 4, v139
	s_mov_b64 exec, s[62:63]
	v_add_u32_e32 v144, 0xe02, v141
	global_store_dword v139, v144, s[40:41]
	v_add_u32_e32 v139, 4, v139
	s_mov_b64 exec, s[64:65]
	v_add_u32_e32 v145, 0xe03, v141
	global_store_dword v139, v145, s[40:41]
	v_add_u32_e32 v139, 4, v139
	s_mov_b64 exec, -1
	s_bcnt1_i32_b64 s4, s[58:59]
	s_add_i32 s26, s26, s4
	s_bcnt1_i32_b64 s4, s[60:61]
	s_add_i32 s26, s26, s4
	s_bcnt1_i32_b64 s4, s[62:63]
	s_add_i32 s26, s26, s4
	s_bcnt1_i32_b64 s4, s[64:65]
	s_add_i32 s26, s26, s4
	s_cmp_le_u32 s79, 15
	s_cbranch_scc1 .Lsel_fsn_bend
	v_cmp_le_u32_e64 s[58:59], v130, s76
	v_cmp_le_u32_e64 s[60:61], v131, s76
	v_cmp_le_u32_e64 s[62:63], v132, s76
	v_cmp_le_u32_e64 s[64:65], v133, s76
	v_mov_b32_e32 v139, s26
	v_mbcnt_lo_u32_b32 v139, s58, v139
	v_mbcnt_hi_u32_b32 v139, s59, v139
	v_mbcnt_lo_u32_b32 v139, s60, v139
	v_mbcnt_hi_u32_b32 v139, s61, v139
	v_mbcnt_lo_u32_b32 v139, s62, v139
	v_mbcnt_hi_u32_b32 v139, s63, v139
	v_mbcnt_lo_u32_b32 v139, s64, v139
	v_mbcnt_hi_u32_b32 v139, s65, v139
	v_lshlrev_b32_e32 v139, 2, v139
	s_mov_b64 exec, s[58:59]
	v_add_u32_e32 v142, 0xf00, v141
	global_store_dword v139, v142, s[40:41]
	v_add_u32_e32 v139, 4, v139
	s_mov_b64 exec, s[60:61]
	v_add_u32_e32 v143, 0xf01, v141
	global_store_dword v139, v143, s[40:41]
	v_add_u32_e32 v139, 4, v139
	s_mov_b64 exec, s[62:63]
	v_add_u32_e32 v144, 0xf02, v141
	global_store_dword v139, v144, s[40:41]
	v_add_u32_e32 v139, 4, v139
	s_mov_b64 exec, s[64:65]
	v_add_u32_e32 v145, 0xf03, v141
	global_store_dword v139, v145, s[40:41]
	v_add_u32_e32 v139, 4, v139
	s_mov_b64 exec, -1
	s_bcnt1_i32_b64 s4, s[58:59]
	s_add_i32 s26, s26, s4
	s_bcnt1_i32_b64 s4, s[60:61]
	s_add_i32 s26, s26, s4
	s_bcnt1_i32_b64 s4, s[62:63]
	s_add_i32 s26, s26, s4
	s_bcnt1_i32_b64 s4, s[64:65]
	s_add_i32 s26, s26, s4
